# P5: issue priority for the waves that build more M blocks per head (4..7)
# speedup vs baseline: 1.0076x; 1.0076x over previous
.LBB0_541:
	v_readlane_b32 s0, v253, 12
	v_readlane_b32 s1, v253, 13
	s_mov_b64 s[4:5], s[0:1]
	s_cmp_lt_i32 s4, 6
	v_readlane_b32 s2, v253, 14
	v_readlane_b32 s3, v253, 15
	s_cselect_b64 s[0:1], -1, 0
	s_cmp_gt_i32 s5, 5
	s_cselect_b64 s[2:3], -1, 0
	s_and_b64 s[0:1], s[0:1], s[2:3]
	v_writelane_b32 v253, s0, 53
	s_andn2_b64 vcc, exec, s[0:1]
	s_nop 0
	v_writelane_b32 v253, s1, 54
	s_cbranch_vccnz .LBB0_600
	s_cmpk_gt_i32 s82, 0x3ff
	s_cbranch_scc1 .LBB0_600
	s_cmp_gt_u32 s84, 3
	s_cbranch_scc0 .Lp5_noprio
	s_setprio 2
.Lp5_noprio:
	v_writelane_b32 v253, s94, 55
	s_add_u32 s0, s92, 0x66100000
	s_addc_u32 s1, s93, 0
	v_writelane_b32 v253, s95, 56
	v_writelane_b32 v253, s0, 57
	s_waitcnt vmcnt(0)
	v_lshlrev_b32_e32 v8, 4, v0
	v_lshrrev_b32_e32 v4, 2, v0
	v_writelane_b32 v253, s1, 58
	s_add_u32 s0, s92, 0x45c00000
	s_addc_u32 s1, s93, 0
	v_writelane_b32 v253, s0, 59
	v_and_b32_e32 v171, 0x78, v4
	v_or_b32_e32 v211, 7, v4
	v_writelane_b32 v253, s1, 60
	v_and_b32_e32 v215, 0x7c, v4
	v_readlane_b32 s0, v253, 18
	v_readlane_b32 s10, v253, 28
	v_readlane_b32 s1, v253, 19
	v_readlane_b32 s11, v253, 29
	s_add_u32 s0, s10, 0x6000
	s_addc_u32 s1, s11, 0
	v_readlane_b32 s2, v253, 20
	v_readlane_b32 s3, v253, 21
	v_readlane_b32 s4, v253, 22
	v_readlane_b32 s5, v253, 23
	v_readlane_b32 s6, v253, 24
	v_readlane_b32 s7, v253, 25
	v_readlane_b32 s8, v253, 26
	v_readlane_b32 s9, v253, 27
	v_readlane_b32 s12, v253, 30
	v_readlane_b32 s13, v253, 31
	v_readlane_b32 s14, v253, 32
	v_readlane_b32 s15, v253, 33
	v_writelane_b32 v253, s0, 61
	v_or_b32_e32 v220, 3, v4
	v_lshlrev_b32_e32 v4, 2, v248
	v_writelane_b32 v253, s1, 62
	s_add_u32 s0, s10, 0xc000
	s_addc_u32 s1, s11, 0
	v_writelane_b32 v253, s0, 63
	v_lshl_or_b32 v4, s84, 9, v4
	v_lshrrev_b32_e32 v12, 4, v248
	v_writelane_b32 v254, s1, 0
	s_add_u32 s0, s10, 0x12000
	s_addc_u32 s1, s11, 0
	v_writelane_b32 v254, s0, 1
	v_add_u32_e32 v221, 0, v4
	v_or_b32_e32 v4, 0x200, v0
	v_writelane_b32 v254, s1, 2
	s_add_i32 s0, 0, 0x1b800
	v_add_u32_e32 v214, s0, v8
	s_add_u32 s0, s92, 0x59c00000
	s_addc_u32 s1, s93, 0
	v_writelane_b32 v254, s0, 3
	s_cmp_gt_u32 s48, 63
	s_cselect_b64 s[4:5], -1, 0
	v_writelane_b32 v254, s1, 4
	v_cmp_gt_u32_e64 s[0:1], 2, v248
	s_cmpk_gt_u32 s48, 0x7f
	v_and_b32_e32 v1, 15, v0
	v_writelane_b32 v254, s0, 5
	v_lshrrev_b32_e32 v4, 4, v4
	v_lshlrev_b32_e32 v164, 2, v12
	v_writelane_b32 v254, s1, 6
	v_cmp_gt_u32_e64 s[0:1], 4, v248
	v_mul_u32_u24_e32 v230, 0x110, v4
	v_lshlrev_b32_e32 v4, 3, v12
	v_writelane_b32 v254, s0, 7
	v_lshl_or_b32 v232, s84, 4, v1
	v_mov_b32_e32 v198, s84
	v_lshrrev_b32_e32 v198, 1, v198
	v_lshlrev_b32_e32 v198, 5, v198
	v_sub_u32_e32 v198, v232, v198
	v_or_b32_e32 v12, 1, v164
	v_writelane_b32 v254, s1, 8
	v_cmp_gt_u32_e64 s[0:1], 8, v248
	v_cmp_eq_u32_e64 s[24:25], v12, v198
	v_or_b32_e32 v12, 3, v164
	v_writelane_b32 v254, s0, 9
	v_or_b32_e32 v13, 17, v164
	v_cmp_gt_u32_e64 s[30:31], v12, v198
	v_writelane_b32 v254, s1, 10
	v_cmp_gt_u32_e64 s[0:1], 16, v248
	v_cmp_eq_u32_e64 s[40:41], v12, v198
	v_or_b32_e32 v12, 33, v164
	v_writelane_b32 v254, s0, 11
	v_cmp_gt_u32_e64 s[18:19], v13, v198
	v_cmp_eq_u32_e64 s[26:27], v13, v198
	v_writelane_b32 v254, s1, 12
	v_cmp_gt_u32_e64 s[0:1], 32, v248
	v_or_b32_e32 v13, 2, v164
	v_or_b32_e32 v14, 16, v164
	v_writelane_b32 v254, s0, 13
	v_cmp_gt_u32_e64 s[34:35], v13, v198
	v_cmp_eq_u32_e64 s[42:43], v13, v198
	v_writelane_b32 v254, s1, 14
	v_writelane_b32 v254, s4, 15
	s_movk_i32 s0, 0x110
	v_mul_lo_u32 v9, v232, s0
	v_writelane_b32 v254, s5, 16
	s_cselect_b64 s[4:5], -1, 0
	v_writelane_b32 v254, s4, 17
	s_cmpk_gt_u32 s48, 0xbf
	v_cmp_gt_u32_e64 s[0:1], v12, v232
	v_writelane_b32 v254, s5, 18
	s_cselect_b64 s[4:5], -1, 0
	v_writelane_b32 v254, s4, 19
	s_cmpk_gt_u32 s48, 0xff
	v_or_b32_e32 v13, 32, v164
	v_writelane_b32 v254, s5, 20
	s_cselect_b64 s[4:5], -1, 0
	v_writelane_b32 v254, s4, 21
	s_cmpk_gt_u32 s48, 0x13f
	v_cmp_gt_u32_e64 s[20:21], v14, v198
	v_writelane_b32 v254, s5, 22
	s_cselect_b64 s[4:5], -1, 0
	v_writelane_b32 v254, s4, 23
	s_cmpk_gt_u32 s48, 0x17f
	v_cmp_eq_u32_e64 s[28:29], v14, v198
	v_writelane_b32 v254, s5, 24
	s_cselect_b64 s[4:5], -1, 0
	v_writelane_b32 v254, s4, 25
	s_cmpk_gt_u32 s48, 0x1bf
	v_or_b32_e32 v14, 19, v164
	v_writelane_b32 v254, s5, 26
	s_cselect_b64 s[4:5], -1, 0
	v_writelane_b32 v254, s4, 27
	v_cmp_gt_u32_e64 s[36:37], v14, v198
	v_cmp_eq_u32_e64 s[44:45], v14, v198
	v_writelane_b32 v254, s5, 28
	v_writelane_b32 v254, s0, 29
	v_or_b32_e32 v14, 49, v164
	v_or_b32_e32 v15, 18, v164
	v_writelane_b32 v254, s1, 30
	v_cmp_gt_u32_e64 s[0:1], v13, v232
	v_cmp_gt_u32_e64 s[38:39], v15, v198
	v_cmp_eq_u32_e64 s[46:47], v15, v198
	v_writelane_b32 v254, s0, 31
	v_or_b32_e32 v15, 48, v164
	v_lshlrev_b32_e32 v2, 1, v0
	v_writelane_b32 v254, s1, 32
	v_cmp_gt_u32_e64 s[0:1], v14, v232
	v_and_b32_e32 v165, 62, v2
	v_lshlrev_b32_e32 v2, 3, v0
	v_writelane_b32 v254, s0, 33
	v_and_b32_e32 v212, 0x78, v2
	v_mov_b32_e32 v161, 0
	v_writelane_b32 v254, s1, 34
	v_cmp_gt_u32_e64 s[0:1], v15, v232
	v_lshlrev_b32_e32 v158, 1, v212
	v_mov_b32_e32 v159, v161
	v_writelane_b32 v254, s0, 35
	v_lshl_add_u64 v[2:3], s[92:93], 0, v[158:159]
	s_add_i32 s33, 0, 0x13000
	v_writelane_b32 v254, s1, 36
	v_cmp_eq_u32_e64 s[0:1], v12, v232
	v_or_b32_e32 v12, 35, v164
	s_add_i32 s10, 0, 0x17400
	v_writelane_b32 v254, s0, 37
	v_and_b32_e32 v160, 0x1f00, v8
	s_cmpk_gt_u32 s48, 0x1ff
	v_writelane_b32 v254, s1, 38
	v_cmp_eq_u32_e64 s[0:1], v13, v232
	v_or_b32_e32 v13, 34, v164
	v_lshl_add_u64 v[2:3], v[2:3], 0, v[160:161]
	v_writelane_b32 v254, s0, 39
	s_cselect_b64 s[94:95], -1, 0
	v_and_b32_e32 v162, 48, v0
	v_writelane_b32 v254, s1, 40
	v_cmp_eq_u32_e64 s[0:1], v14, v232
	v_or_b32_e32 v14, 51, v164
	v_mul_u32_u24_e32 v222, 0x110, v1
	v_writelane_b32 v254, s0, 41
	v_and_b32_e32 v10, 0x1e0, v0
	v_lshrrev_b32_e32 v11, 4, v0
	v_writelane_b32 v254, s1, 42
	v_cmp_eq_u32_e64 s[0:1], v15, v232
	v_or_b32_e32 v15, 50, v164
	v_and_b32_e32 v160, 48, v248
	v_writelane_b32 v254, s0, 43
	v_readlane_b32 s48, v253, 34
	v_add_u32_e32 v159, 0, v8
	v_writelane_b32 v254, s1, 44
	v_cmp_gt_u32_e64 s[0:1], v12, v232
	v_add_u32_e32 v5, 0, v158
	v_mul_u32_u24_e32 v6, 0x110, v215
	v_writelane_b32 v254, s0, 45
	v_mul_u32_u24_e32 v7, 0x110, v220
	v_add3_u32 v223, 0, v162, v222
	v_writelane_b32 v254, s1, 46
	v_cmp_gt_u32_e64 s[0:1], v13, v232
	v_mul_u32_u24_e32 v225, 0x110, v165
	v_lshlrev_b32_e32 v226, 1, v171
	v_writelane_b32 v254, s0, 47
	v_mul_u32_u24_e32 v228, 0x110, v11
	v_add_u32_e32 v9, 0, v9
	v_writelane_b32 v254, s1, 48
	v_cmp_gt_u32_e64 s[0:1], v14, v232
	v_readlane_b32 s49, v253, 35
	v_readlane_b32 s52, v253, 38
	v_writelane_b32 v254, s0, 49
	v_readlane_b32 s53, v253, 39
	v_add_u32_e32 v242, 0, v10
	v_writelane_b32 v254, s1, 50
	v_cmp_gt_u32_e64 s[0:1], v15, v232
	s_mov_b32 s3, 0
	v_add_u32_e32 v213, 0x2000, v159
	v_writelane_b32 v254, s0, 51
	v_add_u32_e32 v208, -2, v215
	v_add_u32_e32 v209, -1, v215
	v_writelane_b32 v254, s1, 52
	v_cmp_eq_u32_e64 s[0:1], v12, v232
	v_or_b32_e32 v12, 0x41, v164
	v_cmp_eq_u32_e64 s[86:87], 0, v248
	v_writelane_b32 v254, s0, 53
	v_add_u32_e32 v224, 0xa800, v223
	v_add3_u32 v227, s33, v225, v226
	v_writelane_b32 v254, s1, 54
	v_cmp_eq_u32_e64 s[0:1], v13, v232
	v_or_b32_e32 v13, 64, v164
	v_add3_u32 v229, s10, v228, v158
	v_writelane_b32 v254, s0, 55
	v_add3_u32 v231, s10, v230, v158
	v_cmp_gt_u32_e64 s[14:15], v198, v164
	v_writelane_b32 v254, s1, 56
	v_cmp_eq_u32_e64 s[0:1], v14, v232
	v_or_b32_e32 v14, 0x51, v164
	v_cmp_gt_u32_e64 s[16:17], v164, v198
	v_writelane_b32 v254, s0, 57
	v_cmp_eq_u32_e64 s[22:23], v164, v198
	v_mov_b32_e32 v207, v248
	v_writelane_b32 v254, s1, 58
	v_cmp_eq_u32_e64 s[0:1], v15, v232
	v_or_b32_e32 v15, 0x50, v164
	v_lshl_add_u64 v[168:169], s[52:53], 0, v[160:161]
	v_writelane_b32 v254, s0, 59
	v_add_u32_e32 v243, 0x200, v242
	s_movk_i32 s11, 0x3000
	v_writelane_b32 v254, s1, 60
	v_cmp_gt_u32_e64 s[0:1], v12, v232
	s_mov_b32 s48, 0x12000
	s_mov_b32 s85, 0x41a00000
	v_writelane_b32 v254, s0, 61
	v_mov_b32_e32 v246, 0x3ecc95a3
	v_add_u32_e32 v247, v5, v6
	v_writelane_b32 v254, s1, 62
	v_cmp_gt_u32_e64 s[0:1], v13, v232
	v_add_u32_e32 v248, v5, v7
	v_add_u32_e32 v249, v9, v162
	v_writelane_b32 v254, s0, 63
	s_mov_b64 s[96:97], 0x80
	v_lshlrev_b32_e32 v172, 1, v4
	v_writelane_b32 v255, s1, 0
	v_cmp_gt_u32_e64 s[0:1], v14, v232
	v_mov_b32_e32 v250, 0x3727c5ac
	v_mov_b32_e32 v174, 0x3f317218
	v_writelane_b32 v255, s0, 1
	v_mov_b32_e32 v251, 0x7f800000
	v_mov_b32_e32 v252, 0x7fc00000
	v_writelane_b32 v255, s1, 2
	v_cmp_gt_u32_e64 s[0:1], v15, v232
	v_mov_b32_e32 v210, 0xff800000
	s_mov_b32 s49, s82
	v_writelane_b32 v255, s0, 3
	v_readlane_b32 s50, v253, 36
	v_readlane_b32 s51, v253, 37
	v_writelane_b32 v255, s1, 4
	v_cmp_eq_u32_e64 s[0:1], v12, v232
	v_or_b32_e32 v12, 0x43, v164
	v_readlane_b32 s54, v253, 40
	v_writelane_b32 v255, s0, 5
	v_readlane_b32 s55, v253, 41
	v_readlane_b32 s56, v253, 42
	v_writelane_b32 v255, s1, 6
	v_cmp_eq_u32_e64 s[0:1], v13, v232
	v_or_b32_e32 v13, 0x42, v164
	v_readlane_b32 s57, v253, 43
	v_writelane_b32 v255, s0, 7
	v_readlane_b32 s58, v253, 44
	v_readlane_b32 s59, v253, 45
	v_writelane_b32 v255, s1, 8
	v_cmp_eq_u32_e64 s[0:1], v14, v232
	v_or_b32_e32 v14, 0x53, v164
	v_readlane_b32 s60, v253, 46
	v_writelane_b32 v255, s0, 9
	v_readlane_b32 s61, v253, 47
	v_readlane_b32 s62, v253, 48
	v_writelane_b32 v255, s1, 10
	v_cmp_eq_u32_e64 s[0:1], v15, v232
	v_or_b32_e32 v15, 0x52, v164
	v_readlane_b32 s63, v253, 49
	v_writelane_b32 v255, s0, 11
	s_nop 1
	v_writelane_b32 v255, s1, 12
	v_cmp_gt_u32_e64 s[0:1], v12, v232
	s_nop 1
	v_writelane_b32 v255, s0, 13
	s_nop 1
	v_writelane_b32 v255, s1, 14
	v_cmp_gt_u32_e64 s[0:1], v13, v232
	s_nop 1
	v_writelane_b32 v255, s0, 15
	s_nop 1
	v_writelane_b32 v255, s1, 16
	v_cmp_gt_u32_e64 s[0:1], v14, v232
	s_nop 1
	v_writelane_b32 v255, s0, 17
	s_nop 1
	v_writelane_b32 v255, s1, 18
	v_cmp_gt_u32_e64 s[0:1], v15, v232
	s_nop 1
	v_writelane_b32 v255, s0, 19
	s_nop 1
	v_writelane_b32 v255, s1, 20
	v_cmp_eq_u32_e64 s[0:1], v12, v232
	v_or_b32_e32 v12, 0x61, v164
	s_nop 0
	v_writelane_b32 v255, s0, 21
	s_nop 1
	v_writelane_b32 v255, s1, 22
	v_cmp_eq_u32_e64 s[0:1], v13, v232
	v_or_b32_e32 v13, 0x60, v164
	s_nop 0
	v_writelane_b32 v255, s0, 23
	s_nop 1
	v_writelane_b32 v255, s1, 24
	v_cmp_eq_u32_e64 s[0:1], v14, v232
	v_or_b32_e32 v14, 0x71, v164
	s_nop 0
	v_writelane_b32 v255, s0, 25
	s_nop 1
	v_writelane_b32 v255, s1, 26
	v_cmp_eq_u32_e64 s[0:1], v15, v232
	v_or_b32_e32 v15, 0x70, v164
	s_nop 0
	v_writelane_b32 v255, s0, 27
	s_nop 1
	v_writelane_b32 v255, s1, 28
	v_cmp_gt_u32_e64 s[0:1], v12, v232
	s_nop 1
	v_writelane_b32 v255, s0, 29
	s_nop 1
	v_writelane_b32 v255, s1, 30
	v_cmp_gt_u32_e64 s[0:1], v13, v232
	s_nop 1
	v_writelane_b32 v255, s0, 31
	s_nop 1
	v_writelane_b32 v255, s1, 32
	v_cmp_gt_u32_e64 s[0:1], v14, v232
	s_nop 1
	v_writelane_b32 v255, s0, 33
	s_nop 1
	v_writelane_b32 v255, s1, 34
	v_cmp_gt_u32_e64 s[0:1], v15, v232
	s_nop 1
	v_writelane_b32 v255, s0, 35
	s_nop 1
	v_writelane_b32 v255, s1, 36
	v_cmp_eq_u32_e64 s[0:1], v12, v232
	v_or_b32_e32 v12, 0x63, v164
	v_cmp_eq_u32_e64 s[72:73], v12, v232
	v_writelane_b32 v255, s0, 37
	s_nop 1
	v_writelane_b32 v255, s1, 38
	v_cmp_eq_u32_e64 s[0:1], v13, v232
	v_or_b32_e32 v13, 0x62, v164
	v_cmp_eq_u32_e64 s[74:75], v13, v232
	v_writelane_b32 v255, s0, 39
	s_nop 1
	v_writelane_b32 v255, s1, 40
	v_cmp_eq_u32_e64 s[0:1], v14, v232
	v_or_b32_e32 v14, 0x73, v164
	v_cmp_eq_u32_e64 s[76:77], v14, v232
	v_writelane_b32 v255, s0, 41
	s_nop 1
	v_writelane_b32 v255, s1, 42
	v_cmp_eq_u32_e64 s[0:1], v15, v232
	v_or_b32_e32 v15, 0x72, v164
	v_cmp_eq_u32_e64 s[78:79], v15, v232
	v_writelane_b32 v255, s0, 43
	s_nop 1
	v_writelane_b32 v255, s1, 44
	v_cmp_gt_u32_e64 s[0:1], v12, v232
	v_mbcnt_lo_u32_b32 v12, -1, 0
	v_mbcnt_hi_u32_b32 v12, -1, v12
	v_writelane_b32 v255, s0, 45
	s_nop 1
	v_writelane_b32 v255, s1, 46
	v_cmp_gt_u32_e64 s[0:1], v13, v232
	v_and_b32_e32 v13, 64, v12
	s_nop 0
	v_writelane_b32 v255, s0, 47
	s_nop 1
	v_writelane_b32 v255, s1, 48
	v_cmp_gt_u32_e64 s[0:1], v14, v232
	v_bfrev_b32_e32 v14, 0.5
	v_lshl_or_b32 v233, v12, 2, v14
	v_add_u32_e32 v14, -1, v12
	v_cmp_lt_i32_e32 vcc, v14, v13
	v_writelane_b32 v255, s0, 49
	s_nop 0
	v_cndmask_b32_e32 v14, v14, v12, vcc
	v_lshlrev_b32_e32 v234, 2, v14
	v_add_u32_e32 v14, -2, v12
	v_cmp_lt_i32_e32 vcc, v14, v13
	v_writelane_b32 v255, s1, 50
	v_cmp_gt_u32_e64 s[0:1], v15, v232
	v_cndmask_b32_e32 v14, v14, v12, vcc
	v_lshlrev_b32_e32 v235, 2, v14
	v_add_u32_e32 v14, -4, v12
	v_cmp_lt_i32_e32 vcc, v14, v13
	v_writelane_b32 v255, s0, 51
	s_nop 0
	v_cndmask_b32_e32 v14, v14, v12, vcc
	v_lshlrev_b32_e32 v236, 2, v14
	v_add_u32_e32 v14, -8, v12
	v_cmp_lt_i32_e32 vcc, v14, v13
	v_writelane_b32 v255, s1, 52
	s_mov_b64 s[0:1], 0x5e000000
	v_cndmask_b32_e32 v14, v14, v12, vcc
	v_lshlrev_b32_e32 v237, 2, v14
	v_add_u32_e32 v14, -16, v12
	v_cmp_lt_i32_e32 vcc, v14, v13
	v_lshl_add_u64 v[166:167], v[2:3], 0, s[0:1]
	s_lshl_b32 s0, s84, 6
	v_cndmask_b32_e32 v14, v14, v12, vcc
	v_lshlrev_b32_e32 v238, 2, v14
	v_subrev_u32_e32 v14, 32, v12
	v_cmp_lt_i32_e32 vcc, v14, v13
	s_add_i32 s0, s0, 0
	v_add_u32_e32 v13, 64, v13
	v_cndmask_b32_e32 v14, v14, v12, vcc
	v_lshlrev_b32_e32 v239, 2, v14
	v_xor_b32_e32 v14, 16, v12
	v_lshl_add_u32 v245, v1, 2, s0
	s_add_u32 s0, s12, 0x100
	v_cmp_lt_i32_e32 vcc, v14, v13
	s_addc_u32 s1, s13, 0
	v_writelane_b32 v255, s0, 53
	v_cndmask_b32_e32 v14, v12, v14, vcc
	v_lshlrev_b32_e32 v240, 2, v14
	v_xor_b32_e32 v14, 32, v12
	v_writelane_b32 v255, s1, 54
	v_cmp_lt_i32_e32 vcc, v14, v13
	v_lshlrev_b32_e32 v2, 4, v1
	v_writelane_b32 v255, s82, 55
	v_cndmask_b32_e32 v12, v12, v14, vcc
	v_lshl_or_b32 v170, v11, 8, v2
	v_add_u32_e32 v2, 0, v160
	v_writelane_b32 v255, s82, 56
	v_lshlrev_b32_e32 v241, 2, v12
	v_add_u32_e32 v244, 0x1000, v2
	s_movk_i32 s12, 0x6000
	s_mov_b32 s13, 0xc000
	v_writelane_b32 v255, s83, 57
	s_branch .LBB0_545

.LBB0_599:
	s_setprio 0
	v_readlane_b32 s94, v253, 55
	v_readlane_b32 s82, v255, 56
	v_readlane_b32 s95, v253, 56
	v_mov_b32_e32 v248, v207
